# v18 plus write-through (sc0 sc1) on pconv2 Y stores to shorten the end-of-kernel flush
# speedup vs baseline: 1.0194x; 1.0194x over previous
.LBB3_2:
	v_cmp_lt_u32_e32 vcc, 12, v20
	s_nop 1
	v_cndmask_b32_e64 v18, 0, -13, vcc
	v_add_u32_e32 v18, v18, v20
	v_lshl_or_b32 v18, v18, 4, v140
	v_cmp_gt_i32_e64 s[0:1], s9, v18
	s_and_saveexec_b64 s[10:11], s[0:1]
	s_cbranch_execz .LBB3_1
	ds_read_b128 v[22:25], v15
	ds_read_b128 v[26:29], v15 offset:26624
	ds_read_b128 v[30:33], v15 offset:53248
	v_add_u32_e32 v21, 0x13800, v15
	ds_read_b128 v[34:37], v21
	v_cndmask_b32_e64 v19, 0, 2, vcc
	s_waitcnt lgkmcnt(2)
	v_pk_add_f32 v[24:25], v[24:25], v[28:29]
	v_pk_add_f32 v[22:23], v[22:23], v[26:27]
	v_or_b32_e32 v21, v19, v13
	v_ashrrev_i32_e32 v19, 31, v18
	s_waitcnt lgkmcnt(1)
	v_pk_add_f32 v[24:25], v[24:25], v[32:33]
	v_pk_add_f32 v[22:23], v[22:23], v[30:31]
	v_lshl_add_u64 v[18:19], v[18:19], 0, s[4:5]
	v_cmp_gt_u32_e32 vcc, 13, v20
	s_waitcnt lgkmcnt(0)
	v_pk_add_f32 v[24:25], v[24:25], v[36:37]
	v_pk_add_f32 v[22:23], v[22:23], v[34:35]
	v_mad_i64_i32 v[18:19], s[0:1], v21, s12, v[18:19]
	v_cndmask_b32_e32 v27, v11, v7, vcc
	v_cndmask_b32_e32 v26, v10, v8, vcc
	v_cndmask_b32_e32 v29, v9, v1, vcc
	v_cndmask_b32_e32 v28, v12, v6, vcc
	v_lshlrev_b64 v[18:19], 5, v[18:19]
	v_pk_fma_f32 v[22:23], v[22:23], s[8:9], v[28:29] op_sel_hi:[1,0,1]
	v_pk_fma_f32 v[24:25], v[24:25], s[8:9], v[26:27] op_sel_hi:[1,0,1]
	v_lshl_add_u64 v[18:19], v[16:17], 0, v[18:19]
	v_pk_fma_f32 v[2:3], v[22:23], v[22:23], v[2:3]
	v_pk_fma_f32 v[4:5], v[24:25], v[24:25], v[4:5]
	global_store_dwordx4 v[18:19], v[22:25], off sc0 sc1
	s_branch .LBB3_1
